# stack10 + widen mid-hook third gate batch issued with the second (into dead B-frag regs) + resid preheader flush removed + scan gamma load overlapped
# baseline (speedup 1.0000x reference)
; #define GAS __attribute__((address_space(1)))
; __device__ __forceinline__ unsigned pk2(float lo, float hi) { f32x2_t_ v = {lo, hi}; bf16x2_t_ b = __builtin_convertvector(v, bf16x2_t_); return __builtin_bit_cast(unsigned, b); }
; __global__ void __launch_bounds__(NWAVES * 64, 2) fwd(Args args) {
;     ...
;             for (int gid = local_ok ? ((((lvcu >> 5) * 4 + (lg_ >> 12)) << 12) + (lg_ & 4095)) : vcu * 512 + tid; gid < 32 * 4096; gid += G * 512) { const int bh = gid >> 12, i4 = gid & 4095; const float dec = __builtin_amdgcn_exp2f(128.f * kLog2Gamma[bh & 7]);
;                 f32x4 S = {0.f, 0.f, 0.f, 0.f};
;                 const GAS f32x4* kp = (const GAS f32x4*)(KV + (size_t)bh * 32 * 16384) + i4; GAS v2u* sp = (GAS v2u*)(SST + (size_t)bh * 32 * 16384) + i4;
;                 f32x4 kc[8], kn[8];
; #pragma unroll
;                 for (int i = 0; i < 8; ++i) kc[i] = kp[(size_t)i * 4096];
; #pragma unroll
;                 for (int r = 0; r < 4; ++r) {
;                     if (r < 3) {
; #pragma unroll
;                         for (int i = 0; i < 8; ++i) if (8 * (r + 1) + i < 31) kn[i] = kp[(size_t)(8 * (r + 1) + i) * 4096]; }
; #pragma unroll
;                     for (int i = 0; i < 8; ++i) if (8 * r + i < 31) { S = S * dec + kc[i]; v2u w; w.x = pk2(S.x, S.y); w.y = pk2(S.z, S.w); sp[(size_t)(8 * r + i + 1) * 4096] = w; }
; #pragma unroll
;                     for (int i = 0; i < 8; ++i) kc[i] = kn[i]; } }
.LBB0_526:
	s_waitcnt vmcnt(0) lgkmcnt(0)
	v_ashrrev_i32_e32 v4, 12, v1
	v_lshlrev_b32_e32 v2, 2, v4
	v_and_b32_e32 v2, 28, v2
	s_getpc_b64 s[18:19]
	s_add_u32 s18, s18, _ZL10kLog2Gamma@rel32@lo+4
	s_addc_u32 s19, s19, _ZL10kLog2Gamma@rel32@hi+12
	global_load_dword v9, v2, s[18:19]
	v_ashrrev_i32_e32 v5, 31, v4
	v_and_b32_e32 v8, 0xfff, v1
	v_lshlrev_b64 v[6:7], 21, v[4:5]
	v_lshl_add_u64 v[6:7], s[50:51], 0, v[6:7]
	v_lshlrev_b64 v[4:5], 20, v[4:5]
	v_lshl_add_u64 v[4:5], s[26:27], 0, v[4:5]
	s_mov_b32 s0, 0x8000
	v_add_u32_e32 v1, s3, v1
	v_lshlrev_b32_e32 v2, 4, v8
	v_lshl_add_u64 v[52:53], v[6:7], 0, v[2:3]
	v_add_co_u32_e32 v6, vcc, s69, v52
	global_load_dwordx4 v[24:27], v[52:53], off
	s_nop 0
	v_addc_co_u32_e32 v7, vcc, 0, v53, vcc
	global_load_dwordx4 v[36:39], v[6:7], off
	v_add_co_u32_e32 v6, vcc, s5, v52
	v_lshlrev_b32_e32 v2, 3, v8
	s_nop 0
	v_addc_co_u32_e32 v7, vcc, 0, v53, vcc
	global_load_dwordx4 v[40:43], v[6:7], off
	v_add_co_u32_e32 v6, vcc, s16, v52
	v_lshl_add_u64 v[48:49], v[4:5], 0, v[2:3]
	s_nop 0
	v_addc_co_u32_e32 v7, vcc, 0, v53, vcc
	global_load_dwordx4 v[54:57], v[6:7], off
	v_add_co_u32_e32 v6, vcc, s24, v52
	s_waitcnt vmcnt(4)
	v_mul_f32_e32 v9, 0x43000000, v9
	v_exp_f32_e32 v50, v9
	s_nop 0
	v_addc_co_u32_e32 v7, vcc, 0, v53, vcc
	global_load_dwordx4 v[58:61], v[6:7], off
	v_add_co_u32_e32 v6, vcc, s25, v52
	s_nop 1
	v_addc_co_u32_e32 v7, vcc, 0, v53, vcc
	global_load_dwordx4 v[62:65], v[6:7], off
	v_add_co_u32_e32 v6, vcc, s34, v52
	s_nop 1
	v_addc_co_u32_e32 v7, vcc, 0, v53, vcc
	global_load_dwordx4 v[66:69], v[6:7], off
	v_add_co_u32_e32 v6, vcc, s42, v52
	s_nop 1
	v_addc_co_u32_e32 v7, vcc, 0, v53, vcc
	global_load_dwordx4 v[70:73], v[6:7], off
	v_add_co_u32_e32 v4, vcc, s43, v52
	s_nop 1
	v_addc_co_u32_e32 v5, vcc, 0, v53, vcc
	global_load_dwordx4 v[44:47], v[4:5], off
	v_add_co_u32_e32 v4, vcc, s44, v52
	s_nop 1
	v_addc_co_u32_e32 v5, vcc, 0, v53, vcc
	global_load_dwordx4 v[32:35], v[4:5], off
	v_add_co_u32_e32 v4, vcc, s45, v52
	s_waitcnt vmcnt(9)
	v_pk_fma_f32 v[26:27], v[50:51], 0, v[26:27] op_sel_hi:[0,0,1]
	v_addc_co_u32_e32 v5, vcc, 0, v53, vcc
	global_load_dwordx4 v[28:31], v[4:5], off
	v_add_co_u32_e32 v4, vcc, s46, v52
	v_pk_fma_f32 v[24:25], v[50:51], 0, v[24:25] op_sel_hi:[0,0,1]
	s_nop 0
	v_addc_co_u32_e32 v5, vcc, 0, v53, vcc
	global_load_dwordx4 v[20:23], v[4:5], off
	v_add_co_u32_e32 v4, vcc, s47, v52
	v_cvt_pk_bf16_f32 v74, v24, v25
	s_nop 0
	v_addc_co_u32_e32 v5, vcc, 0, v53, vcc
	global_load_dwordx4 v[16:19], v[4:5], off
	v_add_co_u32_e32 v4, vcc, s48, v52
	v_cvt_pk_bf16_f32 v75, v26, v27
	s_nop 0
	v_addc_co_u32_e32 v5, vcc, 0, v53, vcc
	global_load_dwordx4 v[12:15], v[4:5], off
	v_add_co_u32_e32 v4, vcc, s49, v52
	s_waitcnt vmcnt(12)
	v_pk_fma_f32 v[26:27], v[50:51], v[26:27], v[38:39] op_sel_hi:[0,1,1]
	v_addc_co_u32_e32 v5, vcc, 0, v53, vcc
	global_load_dwordx4 v[8:11], v[4:5], off
	v_add_co_u32_e32 v4, vcc, s52, v52
	v_pk_fma_f32 v[24:25], v[50:51], v[24:25], v[36:37] op_sel_hi:[0,1,1]
	s_nop 0
	v_addc_co_u32_e32 v5, vcc, 0, v53, vcc
	global_load_dwordx4 v[4:7], v[4:5], off
	v_add_co_u32_e32 v76, vcc, s0, v48
	v_cvt_pk_bf16_f32 v36, v24, v25
	s_nop 0
	v_addc_co_u32_e32 v77, vcc, 0, v49, vcc
	v_add_co_u32_e32 v38, vcc, s69, v48
	v_cvt_pk_bf16_f32 v37, v26, v27
	s_nop 0
	v_addc_co_u32_e32 v39, vcc, 0, v49, vcc
	s_mov_b32 s0, 0x18000
	global_store_dwordx2 v[38:39], v[36:37], off
	s_waitcnt vmcnt(14)
	v_pk_fma_f32 v[26:27], v[50:51], v[26:27], v[42:43] op_sel_hi:[0,1,1]
	v_pk_fma_f32 v[24:25], v[50:51], v[24:25], v[40:41] op_sel_hi:[0,1,1]
	v_add_co_u32_e32 v38, vcc, s0, v48
	v_cvt_pk_bf16_f32 v36, v24, v25
	v_cvt_pk_bf16_f32 v37, v26, v27
	v_addc_co_u32_e32 v39, vcc, 0, v49, vcc
	global_store_dwordx2 v[38:39], v[36:37], off
	s_waitcnt vmcnt(14)
	v_pk_fma_f32 v[26:27], v[50:51], v[26:27], v[56:57] op_sel_hi:[0,1,1]
	v_pk_fma_f32 v[24:25], v[50:51], v[24:25], v[54:55] op_sel_hi:[0,1,1]
	v_add_co_u32_e32 v38, vcc, s5, v48
	v_cvt_pk_bf16_f32 v36, v24, v25
	v_cvt_pk_bf16_f32 v37, v26, v27
	v_addc_co_u32_e32 v39, vcc, 0, v49, vcc
	s_mov_b32 s0, 0x28000
	global_store_dwordx2 v[38:39], v[36:37], off
	s_waitcnt vmcnt(14)
	v_pk_fma_f32 v[26:27], v[50:51], v[26:27], v[60:61] op_sel_hi:[0,1,1]
	v_pk_fma_f32 v[24:25], v[50:51], v[24:25], v[58:59] op_sel_hi:[0,1,1]
	v_add_co_u32_e32 v38, vcc, s0, v48
	v_cvt_pk_bf16_f32 v36, v24, v25
	v_cvt_pk_bf16_f32 v37, v26, v27
	v_addc_co_u32_e32 v39, vcc, 0, v49, vcc
	global_store_dwordx2 v[38:39], v[36:37], off
	s_waitcnt vmcnt(14)
	v_pk_fma_f32 v[26:27], v[50:51], v[26:27], v[64:65] op_sel_hi:[0,1,1]
	v_pk_fma_f32 v[24:25], v[50:51], v[24:25], v[62:63] op_sel_hi:[0,1,1]
	v_add_co_u32_e32 v38, vcc, s16, v48
	v_cvt_pk_bf16_f32 v36, v24, v25
	v_cvt_pk_bf16_f32 v37, v26, v27
	v_addc_co_u32_e32 v39, vcc, 0, v49, vcc
	s_mov_b32 s0, 0x38000
	global_store_dwordx2 v[38:39], v[36:37], off
	v_add_co_u32_e32 v38, vcc, s0, v48
	s_waitcnt vmcnt(14)
	v_pk_fma_f32 v[26:27], v[50:51], v[26:27], v[68:69] op_sel_hi:[0,1,1]
	v_pk_fma_f32 v[24:25], v[50:51], v[24:25], v[66:67] op_sel_hi:[0,1,1]
	v_addc_co_u32_e32 v39, vcc, 0, v49, vcc
	global_store_dwordx2 v[76:77], v[74:75], off
	v_cvt_pk_bf16_f32 v37, v26, v27
	s_waitcnt vmcnt(14)
; __device__ __forceinline__ unsigned pk2(float lo, float hi) { f32x2_t_ v = {lo, hi}; bf16x2_t_ b = __builtin_convertvector(v, bf16x2_t_); return __builtin_bit_cast(unsigned, b); }
; __global__ void __launch_bounds__(NWAVES * 64, 2) fwd(Args args) {
;     ...
;                 for (int r = 0; r < 4; ++r) {
;                     if (r < 3) {
; #pragma unroll
;                         for (int i = 0; i < 8; ++i) if (8 * (r + 1) + i < 31) kn[i] = kp[(size_t)(8 * (r + 1) + i) * 4096]; }
; #pragma unroll
;                     for (int i = 0; i < 8; ++i) if (8 * r + i < 31) { S = S * dec + kc[i]; v2u w; w.x = pk2(S.x, S.y); w.y = pk2(S.z, S.w); sp[(size_t)(8 * r + i + 1) * 4096] = w; }
; #pragma unroll
;                     for (int i = 0; i < 8; ++i) kc[i] = kn[i]; } }
	v_pk_fma_f32 v[74:75], v[50:51], v[26:27], v[72:73] op_sel_hi:[0,1,1]
	v_pk_fma_f32 v[76:77], v[50:51], v[24:25], v[70:71] op_sel_hi:[0,1,1]
	v_add_co_u32_e32 v26, vcc, s24, v48
	v_cvt_pk_bf16_f32 v36, v24, v25
	v_cvt_pk_bf16_f32 v24, v76, v77
	v_cvt_pk_bf16_f32 v25, v74, v75
	v_addc_co_u32_e32 v27, vcc, 0, v49, vcc
	s_mov_b32 s0, 0x100000
	global_store_dwordx2 v[26:27], v[24:25], off
	v_add_co_u32_e32 v24, vcc, s0, v52
	global_store_dwordx2 v[38:39], v[36:37], off
	s_nop 0
	v_addc_co_u32_e32 v25, vcc, 0, v53, vcc
	s_mov_b32 s0, 0x110000
	global_load_dwordx4 v[54:57], v[24:25], off
	v_add_co_u32_e32 v24, vcc, s0, v52
	s_mov_b32 s0, 0x120000
	s_nop 0
	v_addc_co_u32_e32 v25, vcc, 0, v53, vcc
	global_load_dwordx4 v[58:61], v[24:25], off
	v_add_co_u32_e32 v24, vcc, s0, v52
	s_mov_b32 s0, 0x130000
	s_nop 0
	v_addc_co_u32_e32 v25, vcc, 0, v53, vcc
	global_load_dwordx4 v[62:65], v[24:25], off
	v_add_co_u32_e32 v24, vcc, s0, v52
	s_mov_b32 s0, 0x140000
	s_nop 0
	v_addc_co_u32_e32 v25, vcc, 0, v53, vcc
	global_load_dwordx4 v[66:69], v[24:25], off
	v_add_co_u32_e32 v24, vcc, s0, v52
	s_mov_b32 s0, 0x150000
	s_nop 0
	v_addc_co_u32_e32 v25, vcc, 0, v53, vcc
	global_load_dwordx4 v[70:73], v[24:25], off
	v_add_co_u32_e32 v24, vcc, s0, v52
	s_mov_b32 s0, 0x160000
	s_nop 0
	v_addc_co_u32_e32 v25, vcc, 0, v53, vcc
	global_load_dwordx4 v[36:39], v[24:25], off
	v_add_co_u32_e32 v24, vcc, s0, v52
	s_mov_b32 s0, 0x170000
	s_nop 0
	v_addc_co_u32_e32 v25, vcc, 0, v53, vcc
	global_load_dwordx4 v[40:43], v[24:25], off
	v_add_co_u32_e32 v24, vcc, s0, v52
	s_mov_b32 s0, 0x48000
	s_nop 0
	v_addc_co_u32_e32 v25, vcc, 0, v53, vcc
	s_waitcnt vmcnt(22)
	v_pk_fma_f32 v[44:45], v[50:51], v[76:77], v[44:45] op_sel_hi:[0,1,1]
	v_add_co_u32_e32 v76, vcc, s0, v48
	v_pk_fma_f32 v[46:47], v[50:51], v[74:75], v[46:47] op_sel_hi:[0,1,1]
	s_nop 0
	v_addc_co_u32_e32 v77, vcc, 0, v49, vcc
	v_cvt_pk_bf16_f32 v75, v46, v47
	s_waitcnt vmcnt(21)
	v_pk_fma_f32 v[34:35], v[50:51], v[46:47], v[34:35] op_sel_hi:[0,1,1]
	v_add_co_u32_e32 v46, vcc, s25, v48
	s_mov_b32 s0, 0x58000
	s_nop 0
	v_addc_co_u32_e32 v47, vcc, 0, v49, vcc
	v_cvt_pk_bf16_f32 v74, v44, v45
	v_pk_fma_f32 v[32:33], v[50:51], v[44:45], v[32:33] op_sel_hi:[0,1,1]
	v_cvt_pk_bf16_f32 v45, v34, v35
	s_waitcnt vmcnt(20)
	v_pk_fma_f32 v[30:31], v[50:51], v[34:35], v[30:31] op_sel_hi:[0,1,1]
	v_add_co_u32_e32 v34, vcc, s0, v48
	v_cvt_pk_bf16_f32 v44, v32, v33
	s_nop 0
	v_addc_co_u32_e32 v35, vcc, 0, v49, vcc
	v_pk_fma_f32 v[28:29], v[50:51], v[32:33], v[28:29] op_sel_hi:[0,1,1]
	v_cvt_pk_bf16_f32 v33, v30, v31
	s_waitcnt vmcnt(19)
	v_pk_fma_f32 v[22:23], v[50:51], v[30:31], v[22:23] op_sel_hi:[0,1,1]
	v_add_co_u32_e32 v30, vcc, s34, v48
	s_mov_b32 s0, 0x68000
	s_nop 0
	v_addc_co_u32_e32 v31, vcc, 0, v49, vcc
	v_cvt_pk_bf16_f32 v32, v28, v29
	v_pk_fma_f32 v[20:21], v[50:51], v[28:29], v[20:21] op_sel_hi:[0,1,1]
	v_cvt_pk_bf16_f32 v29, v22, v23
	s_waitcnt vmcnt(18)
	v_pk_fma_f32 v[18:19], v[50:51], v[22:23], v[18:19] op_sel_hi:[0,1,1]
	v_add_co_u32_e32 v22, vcc, s0, v48
	v_cvt_pk_bf16_f32 v28, v20, v21
	s_nop 0
	v_addc_co_u32_e32 v23, vcc, 0, v49, vcc
	v_pk_fma_f32 v[16:17], v[50:51], v[20:21], v[16:17] op_sel_hi:[0,1,1]
	v_cvt_pk_bf16_f32 v21, v18, v19
	s_waitcnt vmcnt(17)
	v_pk_fma_f32 v[14:15], v[50:51], v[18:19], v[14:15] op_sel_hi:[0,1,1]
	v_add_co_u32_e32 v18, vcc, s42, v48
	s_mov_b32 s0, 0x78000
	s_nop 0
	v_addc_co_u32_e32 v19, vcc, 0, v49, vcc
	v_cvt_pk_bf16_f32 v20, v16, v17
	v_pk_fma_f32 v[12:13], v[50:51], v[16:17], v[12:13] op_sel_hi:[0,1,1]
	v_cvt_pk_bf16_f32 v17, v14, v15
	s_waitcnt vmcnt(16)
	v_pk_fma_f32 v[10:11], v[50:51], v[14:15], v[10:11] op_sel_hi:[0,1,1]
	v_add_co_u32_e32 v14, vcc, s0, v48
	v_pk_fma_f32 v[8:9], v[50:51], v[12:13], v[8:9] op_sel_hi:[0,1,1]
	s_nop 0
	v_addc_co_u32_e32 v15, vcc, 0, v49, vcc
	global_load_dwordx4 v[24:27], v[24:25], off
	s_mov_b32 s0, 0x180000
	global_store_dwordx2 v[46:47], v[44:45], off
	s_waitcnt vmcnt(17)
	v_pk_fma_f32 v[44:45], v[50:51], v[10:11], v[6:7] op_sel_hi:[0,1,1]
	v_pk_fma_f32 v[46:47], v[50:51], v[8:9], v[4:5] op_sel_hi:[0,1,1]
	v_add_co_u32_e32 v6, vcc, s43, v48
	v_cvt_pk_bf16_f32 v4, v46, v47
	v_cvt_pk_bf16_f32 v5, v44, v45
	v_addc_co_u32_e32 v7, vcc, 0, v49, vcc
	global_store_dwordx2 v[6:7], v[4:5], off
	v_add_co_u32_e32 v4, vcc, s0, v52
	v_cvt_pk_bf16_f32 v16, v12, v13
	v_cvt_pk_bf16_f32 v12, v8, v9
	v_cvt_pk_bf16_f32 v13, v10, v11
	v_addc_co_u32_e32 v5, vcc, 0, v53, vcc
	s_mov_b32 s0, 0x190000
	global_store_dwordx2 v[76:77], v[74:75], off
	global_store_dwordx2 v[34:35], v[32:33], off
	global_store_dwordx2 v[30:31], v[28:29], off
	global_store_dwordx2 v[22:23], v[20:21], off
	global_store_dwordx2 v[18:19], v[16:17], off
	global_store_dwordx2 v[14:15], v[12:13], off
	v_add_co_u32_e32 v8, vcc, s0, v52
	global_load_dwordx4 v[4:7], v[4:5], off
	s_nop 0
	v_addc_co_u32_e32 v9, vcc, 0, v53, vcc
	s_mov_b32 s0, 0x1a0000
	v_add_co_u32_e32 v12, vcc, s0, v52
	global_load_dwordx4 v[8:11], v[8:9], off
	s_nop 0
	v_addc_co_u32_e32 v13, vcc, 0, v53, vcc
	s_mov_b32 s0, 0x1b0000
	v_add_co_u32_e32 v16, vcc, s0, v52
	global_load_dwordx4 v[12:15], v[12:13], off
	s_nop 0
	v_addc_co_u32_e32 v17, vcc, 0, v53, vcc
	s_mov_b32 s0, 0x1c0000
	v_add_co_u32_e32 v20, vcc, s0, v52
	global_load_dwordx4 v[16:19], v[16:17], off
	s_nop 0
	v_addc_co_u32_e32 v21, vcc, 0, v53, vcc
	s_mov_b32 s0, 0x1d0000
	v_add_co_u32_e32 v28, vcc, s0, v52
	global_load_dwordx4 v[20:23], v[20:21], off
	s_nop 0
	v_addc_co_u32_e32 v29, vcc, 0, v53, vcc
	s_mov_b32 s0, 0x1e0000
	v_add_co_u32_e32 v32, vcc, s0, v52
	global_load_dwordx4 v[28:31], v[28:29], off
	s_nop 0
	v_addc_co_u32_e32 v33, vcc, 0, v53, vcc
	global_load_dwordx4 v[32:35], v[32:33], off
	s_mov_b32 s0, 0x88000
	s_waitcnt vmcnt(22)
; __device__ __forceinline__ unsigned pk2(float lo, float hi) { f32x2_t_ v = {lo, hi}; bf16x2_t_ b = __builtin_convertvector(v, bf16x2_t_); return __builtin_bit_cast(unsigned, b); }
; __global__ void __launch_bounds__(NWAVES * 64, 2) fwd(Args args) {
;     ...
;                 for (int r = 0; r < 4; ++r) {
;                     if (r < 3) {
; #pragma unroll
;                         for (int i = 0; i < 8; ++i) if (8 * (r + 1) + i < 31) kn[i] = kp[(size_t)(8 * (r + 1) + i) * 4096]; }
; #pragma unroll
;                     for (int i = 0; i < 8; ++i) if (8 * r + i < 31) { S = S * dec + kc[i]; v2u w; w.x = pk2(S.x, S.y); w.y = pk2(S.z, S.w); sp[(size_t)(8 * r + i + 1) * 4096] = w; }
; #pragma unroll
;                     for (int i = 0; i < 8; ++i) kc[i] = kn[i]; } }
	v_pk_fma_f32 v[44:45], v[50:51], v[44:45], v[56:57] op_sel_hi:[0,1,1]
	v_pk_fma_f32 v[46:47], v[50:51], v[46:47], v[54:55] op_sel_hi:[0,1,1]
	v_add_co_u32_e32 v54, vcc, s0, v48
	v_cvt_pk_bf16_f32 v52, v46, v47
	v_cvt_pk_bf16_f32 v53, v44, v45
	v_addc_co_u32_e32 v55, vcc, 0, v49, vcc
	global_store_dwordx2 v[54:55], v[52:53], off
	s_waitcnt vmcnt(22)
	v_pk_fma_f32 v[44:45], v[50:51], v[44:45], v[60:61] op_sel_hi:[0,1,1]
	v_pk_fma_f32 v[46:47], v[50:51], v[46:47], v[58:59] op_sel_hi:[0,1,1]
	v_add_co_u32_e32 v54, vcc, s44, v48
	v_cvt_pk_bf16_f32 v52, v46, v47
	v_cvt_pk_bf16_f32 v53, v44, v45
	v_addc_co_u32_e32 v55, vcc, 0, v49, vcc
	s_mov_b32 s0, 0x98000
	global_store_dwordx2 v[54:55], v[52:53], off
	s_waitcnt vmcnt(22)
	v_pk_fma_f32 v[44:45], v[50:51], v[44:45], v[64:65] op_sel_hi:[0,1,1]
	v_pk_fma_f32 v[46:47], v[50:51], v[46:47], v[62:63] op_sel_hi:[0,1,1]
	v_add_co_u32_e32 v54, vcc, s0, v48
	v_cvt_pk_bf16_f32 v52, v46, v47
	v_cvt_pk_bf16_f32 v53, v44, v45
	v_addc_co_u32_e32 v55, vcc, 0, v49, vcc
	global_store_dwordx2 v[54:55], v[52:53], off
	s_waitcnt vmcnt(22)
	v_pk_fma_f32 v[44:45], v[50:51], v[44:45], v[68:69] op_sel_hi:[0,1,1]
	v_pk_fma_f32 v[46:47], v[50:51], v[46:47], v[66:67] op_sel_hi:[0,1,1]
	v_add_co_u32_e32 v54, vcc, s45, v48
	v_cvt_pk_bf16_f32 v52, v46, v47
	v_cvt_pk_bf16_f32 v53, v44, v45
	v_addc_co_u32_e32 v55, vcc, 0, v49, vcc
	s_mov_b32 s0, 0xa8000
	global_store_dwordx2 v[54:55], v[52:53], off
	v_add_co_u32_e32 v54, vcc, s0, v48
	s_waitcnt vmcnt(22)
	v_pk_fma_f32 v[46:47], v[50:51], v[46:47], v[70:71] op_sel_hi:[0,1,1]
	v_addc_co_u32_e32 v55, vcc, 0, v49, vcc
	v_pk_fma_f32 v[44:45], v[50:51], v[44:45], v[72:73] op_sel_hi:[0,1,1]
	v_cvt_pk_bf16_f32 v52, v46, v47
	s_waitcnt vmcnt(21)
	v_pk_fma_f32 v[36:37], v[50:51], v[46:47], v[36:37] op_sel_hi:[0,1,1]
	v_add_co_u32_e32 v46, vcc, s46, v48
	v_pk_fma_f32 v[38:39], v[50:51], v[44:45], v[38:39] op_sel_hi:[0,1,1]
	s_nop 0
	v_addc_co_u32_e32 v47, vcc, 0, v49, vcc
	s_mov_b32 s0, 0xb8000
	v_cvt_pk_bf16_f32 v53, v44, v45
	v_cvt_pk_bf16_f32 v45, v38, v39
	s_waitcnt vmcnt(20)
	v_pk_fma_f32 v[38:39], v[50:51], v[38:39], v[42:43] op_sel_hi:[0,1,1]
	v_add_co_u32_e32 v42, vcc, s0, v48
	v_cvt_pk_bf16_f32 v44, v36, v37
	s_nop 0
	v_addc_co_u32_e32 v43, vcc, 0, v49, vcc
	v_pk_fma_f32 v[36:37], v[50:51], v[36:37], v[40:41] op_sel_hi:[0,1,1]
	v_cvt_pk_bf16_f32 v41, v38, v39
	s_waitcnt vmcnt(19)
	v_pk_fma_f32 v[26:27], v[50:51], v[38:39], v[26:27] op_sel_hi:[0,1,1]
	v_add_co_u32_e32 v38, vcc, s47, v48
	s_mov_b32 s0, 0xc8000
	s_nop 0
	v_addc_co_u32_e32 v39, vcc, 0, v49, vcc
	v_cvt_pk_bf16_f32 v40, v36, v37
	v_pk_fma_f32 v[24:25], v[50:51], v[36:37], v[24:25] op_sel_hi:[0,1,1]
	v_cvt_pk_bf16_f32 v37, v26, v27
	s_waitcnt vmcnt(10)
	v_pk_fma_f32 v[6:7], v[50:51], v[26:27], v[6:7] op_sel_hi:[0,1,1]
	v_add_co_u32_e32 v26, vcc, s0, v48
	v_pk_fma_f32 v[4:5], v[50:51], v[24:25], v[4:5] op_sel_hi:[0,1,1]
	s_nop 0
	v_addc_co_u32_e32 v27, vcc, 0, v49, vcc
	v_cvt_pk_bf16_f32 v36, v24, v25
	v_cvt_pk_bf16_f32 v24, v4, v5
	v_cvt_pk_bf16_f32 v25, v6, v7
	s_waitcnt vmcnt(9)
	v_pk_fma_f32 v[6:7], v[50:51], v[6:7], v[10:11] op_sel_hi:[0,1,1]
	v_pk_fma_f32 v[4:5], v[50:51], v[4:5], v[8:9] op_sel_hi:[0,1,1]
	v_add_co_u32_e32 v10, vcc, s48, v48
	v_cvt_pk_bf16_f32 v8, v4, v5
	v_cvt_pk_bf16_f32 v9, v6, v7
	v_addc_co_u32_e32 v11, vcc, 0, v49, vcc
	s_mov_b32 s0, 0xd8000
	global_store_dwordx2 v[10:11], v[8:9], off
	s_waitcnt vmcnt(9)
	v_pk_fma_f32 v[6:7], v[50:51], v[6:7], v[14:15] op_sel_hi:[0,1,1]
	v_pk_fma_f32 v[4:5], v[50:51], v[4:5], v[12:13] op_sel_hi:[0,1,1]
	v_add_co_u32_e32 v10, vcc, s0, v48
	v_cvt_pk_bf16_f32 v8, v4, v5
	v_cvt_pk_bf16_f32 v9, v6, v7
	v_addc_co_u32_e32 v11, vcc, 0, v49, vcc
	global_store_dwordx2 v[10:11], v[8:9], off
	s_waitcnt vmcnt(9)
	v_pk_fma_f32 v[6:7], v[50:51], v[6:7], v[18:19] op_sel_hi:[0,1,1]
	v_pk_fma_f32 v[4:5], v[50:51], v[4:5], v[16:17] op_sel_hi:[0,1,1]
	v_add_co_u32_e32 v10, vcc, s49, v48
	v_cvt_pk_bf16_f32 v8, v4, v5
	v_cvt_pk_bf16_f32 v9, v6, v7
	v_addc_co_u32_e32 v11, vcc, 0, v49, vcc
	s_mov_b32 s0, 0xe8000
	global_store_dwordx2 v[10:11], v[8:9], off
	s_waitcnt vmcnt(9)
	v_pk_fma_f32 v[6:7], v[50:51], v[6:7], v[22:23] op_sel_hi:[0,1,1]
	v_pk_fma_f32 v[4:5], v[50:51], v[4:5], v[20:21] op_sel_hi:[0,1,1]
	v_add_co_u32_e32 v10, vcc, s0, v48
	v_cvt_pk_bf16_f32 v8, v4, v5
	v_cvt_pk_bf16_f32 v9, v6, v7
	v_addc_co_u32_e32 v11, vcc, 0, v49, vcc
	global_store_dwordx2 v[10:11], v[8:9], off
	s_waitcnt vmcnt(9)
	v_pk_fma_f32 v[6:7], v[50:51], v[6:7], v[30:31] op_sel_hi:[0,1,1]
	v_pk_fma_f32 v[4:5], v[50:51], v[4:5], v[28:29] op_sel_hi:[0,1,1]
	v_add_co_u32_e32 v10, vcc, s52, v48
	v_cvt_pk_bf16_f32 v8, v4, v5
	v_cvt_pk_bf16_f32 v9, v6, v7
	v_addc_co_u32_e32 v11, vcc, 0, v49, vcc
	s_waitcnt vmcnt(8)
	v_pk_fma_f32 v[6:7], v[50:51], v[6:7], v[34:35] op_sel_hi:[0,1,1]
	v_pk_fma_f32 v[4:5], v[50:51], v[4:5], v[32:33] op_sel_hi:[0,1,1]
	v_cvt_pk_bf16_f32 v4, v4, v5
	v_cvt_pk_bf16_f32 v5, v6, v7
	v_add_co_u32_e32 v6, vcc, 0xf8000, v48
	s_mov_b32 s0, 0x1ffff
	s_nop 0
	v_addc_co_u32_e32 v7, vcc, 0, v49, vcc
	v_cmp_lt_i32_e32 vcc, s0, v1
	s_or_b64 s[40:41], vcc, s[40:41]
	global_store_dwordx2 v[54:55], v[52:53], off
	global_store_dwordx2 v[46:47], v[44:45], off
	global_store_dwordx2 v[42:43], v[40:41], off
	global_store_dwordx2 v[38:39], v[36:37], off
	global_store_dwordx2 v[26:27], v[24:25], off
	global_store_dwordx2 v[10:11], v[8:9], off
	global_store_dwordx2 v[6:7], v[4:5], off
	s_andn2_b64 exec, exec, s[40:41]
	s_cbranch_execnz .LBB0_526

;     static __device__ __forceinline__ float ub(unsigned w, int k) { return (float)((w >> (8 * k)) & 255u); }
;     __device__ __forceinline__ void mid(f32x4 (&acc)[2][2][4][2], const Unit& u, int t, int wr, int wc, int fr, int fq) const {
;         const int row0 = u.pm * BM + wr * 64 + fr, col0 = u.pn * BM + wc * 32 + 8 * fq;
;         const unsigned char* gp = G + (t == MID_T0 ? 0 : 2048) + col0 + (size_t)row0 * ldg;
; #pragma unroll
;         for (int ai = 0; ai < 2; ++ai) { u32x2 ga[4][2], gb[4][2];
; #pragma unroll
;             for (int m = 0; m < 4; ++m)
; #pragma unroll
;                 for (int bj = 0; bj < 2; ++bj) { const unsigned char* p = gp + (size_t)(ai * HALF + m * 16) * ldg + bj * HALF; ga[m][bj] = *(const u32x2*)p; gb[m][bj] = *(const u32x2*)(p + 2048); }
; #pragma unroll
;             for (int m = 0; m < 4; ++m)
; #pragma unroll
;                 for (int bj = 0; bj < 2; ++bj)
; #pragma unroll
;                     for (int h = 0; h < 2; ++h)
; #pragma unroll
;                         for (int k = 0; k < 4; ++k) acc[ai][bj][m][h][k] *= ub(ga[m][bj][h], k) * __builtin_amdgcn_rcpf(ub(gb[m][bj][h], k));
.LBB0_776:
	s_cmpk_eq_i32 s58, 0x800
	s_cselect_b32 s34, 0, 0x800
	v_lshl_add_u64 v[4:5], v[224:225], 0, s[34:35]
	global_load_dwordx2 v[162:163], v[4:5], off
	global_load_dwordx2 v[164:165], v[4:5], off offset:2048
	global_load_dwordx2 v[158:159], v[4:5], off offset:128
	global_load_dwordx2 v[160:161], v[4:5], off offset:2176
	v_add_co_u32_e32 v134, vcc, 0x70000, v4
	s_mov_b32 s0, 0x380000
	s_nop 0
	v_addc_co_u32_e32 v135, vcc, 0, v5, vcc
	global_load_dwordx2 v[154:155], v[134:135], off
	global_load_dwordx2 v[156:157], v[134:135], off offset:2048
	global_load_dwordx2 v[150:151], v[134:135], off offset:128
	global_load_dwordx2 v[152:153], v[134:135], off offset:2176
	v_add_co_u32_e32 v134, vcc, 0xe0000, v4
	s_waitcnt vmcnt(0)
	v_cvt_f32_ubyte1_e32 v173, v162
	v_addc_co_u32_e32 v135, vcc, 0, v5, vcc
	global_load_dwordx2 v[146:147], v[134:135], off
	global_load_dwordx2 v[148:149], v[134:135], off offset:2048
	global_load_dwordx2 v[138:139], v[134:135], off offset:128
	global_load_dwordx2 v[142:143], v[134:135], off offset:2176
	v_add_co_u32_e32 v136, vcc, 0x150000, v4
	v_cvt_f32_ubyte0_e32 v2, v164
	s_nop 0
	v_addc_co_u32_e32 v137, vcc, 0, v5, vcc
	global_load_dwordx2 v[140:141], v[136:137], off
	global_load_dwordx2 v[144:145], v[136:137], off offset:2048
	global_load_dwordx2 v[134:135], v[136:137], off offset:128
	s_nop 0
	global_load_dwordx2 v[136:137], v[136:137], off offset:2176
	s_mov_b32 s101, 0
	s_mov_b32 s100, 0x380000
	v_lshl_add_u64 v[196:197], v[4:5], 0, s[100:101]
	global_load_dwordx2 v[174:175], v[196:197], off
	global_load_dwordx2 v[176:177], v[196:197], off offset:2048
	global_load_dwordx2 v[178:179], v[196:197], off offset:128
	global_load_dwordx2 v[180:181], v[196:197], off offset:2176
	s_mov_b32 s100, 0x3f0000
	v_lshl_add_u64 v[196:197], v[4:5], 0, s[100:101]
	global_load_dwordx2 v[182:183], v[196:197], off
	global_load_dwordx2 v[184:185], v[196:197], off offset:2048
	global_load_dwordx2 v[186:187], v[196:197], off offset:128
	global_load_dwordx2 v[188:189], v[196:197], off offset:2176
	s_mov_b32 s100, 0x460000
	v_lshl_add_u64 v[196:197], v[4:5], 0, s[100:101]
	global_load_dwordx2 v[190:191], v[196:197], off
	global_load_dwordx2 v[192:193], v[196:197], off offset:2048
	global_load_dwordx2 v[194:195], v[196:197], off offset:128
	global_load_dwordx2 v[196:197], v[196:197], off offset:2176
	v_rcp_iflag_f32_e32 v166, v2
	v_cvt_f32_ubyte1_e32 v2, v164
	v_rcp_iflag_f32_e32 v167, v2
	v_cvt_f32_ubyte2_e32 v2, v164
	v_rcp_iflag_f32_e32 v168, v2
	v_cvt_f32_ubyte3_e32 v2, v164
	v_cvt_f32_ubyte0_e32 v172, v162
	v_rcp_iflag_f32_e32 v169, v2
	v_pk_mul_f32 v[166:167], v[166:167], v[172:173]
	v_cvt_f32_ubyte0_e32 v2, v165
	v_pk_mul_f32 v[130:131], v[130:131], v[166:167]
	v_rcp_iflag_f32_e32 v166, v2
	v_cvt_f32_ubyte1_e32 v2, v165
	v_rcp_iflag_f32_e32 v167, v2
	v_cvt_f32_ubyte3_e32 v171, v162
	v_cvt_f32_ubyte2_e32 v170, v162
	v_cvt_f32_ubyte2_e32 v2, v165
	v_pk_mul_f32 v[168:169], v[168:169], v[170:171]
	v_rcp_iflag_f32_e32 v164, v2
	v_cvt_f32_ubyte3_e32 v2, v165
	v_cvt_f32_ubyte1_e32 v171, v163
	v_cvt_f32_ubyte0_e32 v170, v163
	v_pk_mul_f32 v[132:133], v[132:133], v[168:169]
	v_rcp_iflag_f32_e32 v165, v2
	v_cvt_f32_ubyte3_e32 v169, v163
	v_cvt_f32_ubyte2_e32 v168, v163
	v_pk_mul_f32 v[162:163], v[166:167], v[170:171]
	v_cvt_f32_ubyte0_e32 v2, v160
	v_pk_mul_f32 v[126:127], v[126:127], v[162:163]
	v_rcp_iflag_f32_e32 v162, v2
	v_cvt_f32_ubyte1_e32 v2, v160
	v_rcp_iflag_f32_e32 v163, v2
	v_pk_mul_f32 v[164:165], v[164:165], v[168:169]
	v_cvt_f32_ubyte2_e32 v2, v160
	v_pk_mul_f32 v[128:129], v[128:129], v[164:165]
	v_rcp_iflag_f32_e32 v164, v2
	v_cvt_f32_ubyte3_e32 v2, v160
	v_cvt_f32_ubyte1_e32 v169, v158
	v_cvt_f32_ubyte0_e32 v168, v158
	v_rcp_iflag_f32_e32 v165, v2
	v_pk_mul_f32 v[162:163], v[162:163], v[168:169]
	v_cvt_f32_ubyte0_e32 v2, v161
	v_pk_mul_f32 v[122:123], v[122:123], v[162:163]
	v_rcp_iflag_f32_e32 v162, v2
	v_cvt_f32_ubyte1_e32 v2, v161
	v_rcp_iflag_f32_e32 v163, v2
	v_cvt_f32_ubyte3_e32 v167, v158
	v_cvt_f32_ubyte2_e32 v166, v158
	v_cvt_f32_ubyte2_e32 v2, v161
	v_pk_mul_f32 v[164:165], v[164:165], v[166:167]
	v_rcp_iflag_f32_e32 v160, v2
	v_cvt_f32_ubyte3_e32 v2, v161
	v_cvt_f32_ubyte1_e32 v167, v159
	v_cvt_f32_ubyte0_e32 v166, v159
	v_pk_mul_f32 v[124:125], v[124:125], v[164:165]
	v_rcp_iflag_f32_e32 v161, v2
	v_cvt_f32_ubyte3_e32 v165, v159
	v_cvt_f32_ubyte2_e32 v164, v159
	v_pk_mul_f32 v[158:159], v[162:163], v[166:167]
	v_cvt_f32_ubyte0_e32 v2, v156
	v_pk_mul_f32 v[118:119], v[118:119], v[158:159]
	v_rcp_iflag_f32_e32 v158, v2
	v_cvt_f32_ubyte1_e32 v2, v156
	v_rcp_iflag_f32_e32 v159, v2
	v_pk_mul_f32 v[160:161], v[160:161], v[164:165]
	v_cvt_f32_ubyte2_e32 v2, v156
	v_pk_mul_f32 v[120:121], v[120:121], v[160:161]
	v_rcp_iflag_f32_e32 v160, v2
	v_cvt_f32_ubyte3_e32 v2, v156
	v_cvt_f32_ubyte1_e32 v165, v154
	v_cvt_f32_ubyte0_e32 v164, v154
	v_rcp_iflag_f32_e32 v161, v2
	v_pk_mul_f32 v[158:159], v[158:159], v[164:165]
	v_cvt_f32_ubyte0_e32 v2, v157
	v_pk_mul_f32 v[114:115], v[114:115], v[158:159]
	v_rcp_iflag_f32_e32 v158, v2
	v_cvt_f32_ubyte1_e32 v2, v157
	v_rcp_iflag_f32_e32 v159, v2
	v_cvt_f32_ubyte3_e32 v163, v154
	v_cvt_f32_ubyte2_e32 v162, v154
	v_cvt_f32_ubyte2_e32 v2, v157
	v_pk_mul_f32 v[160:161], v[160:161], v[162:163]
	v_rcp_iflag_f32_e32 v156, v2
	v_cvt_f32_ubyte3_e32 v2, v157
	v_cvt_f32_ubyte1_e32 v163, v155
	v_cvt_f32_ubyte0_e32 v162, v155
	v_pk_mul_f32 v[116:117], v[116:117], v[160:161]
	v_rcp_iflag_f32_e32 v157, v2
	v_cvt_f32_ubyte3_e32 v161, v155
	v_cvt_f32_ubyte2_e32 v160, v155
	v_pk_mul_f32 v[154:155], v[158:159], v[162:163]
	v_cvt_f32_ubyte0_e32 v2, v152
	v_pk_mul_f32 v[110:111], v[110:111], v[154:155]
	v_rcp_iflag_f32_e32 v154, v2
	v_cvt_f32_ubyte1_e32 v2, v152
	v_rcp_iflag_f32_e32 v155, v2
	v_pk_mul_f32 v[156:157], v[156:157], v[160:161]
	v_cvt_f32_ubyte2_e32 v2, v152
	v_pk_mul_f32 v[112:113], v[112:113], v[156:157]
	v_rcp_iflag_f32_e32 v156, v2
	v_cvt_f32_ubyte3_e32 v2, v152
	v_cvt_f32_ubyte1_e32 v161, v150
	v_cvt_f32_ubyte0_e32 v160, v150
	v_rcp_iflag_f32_e32 v157, v2
	v_pk_mul_f32 v[154:155], v[154:155], v[160:161]
	v_cvt_f32_ubyte0_e32 v2, v153
	v_pk_mul_f32 v[106:107], v[106:107], v[154:155]
	v_rcp_iflag_f32_e32 v154, v2
	v_cvt_f32_ubyte1_e32 v2, v153
	v_rcp_iflag_f32_e32 v155, v2
	v_cvt_f32_ubyte3_e32 v159, v150
	v_cvt_f32_ubyte2_e32 v158, v150
	v_cvt_f32_ubyte2_e32 v2, v153
	v_pk_mul_f32 v[156:157], v[156:157], v[158:159]
	v_rcp_iflag_f32_e32 v152, v2
	v_cvt_f32_ubyte3_e32 v2, v153
	v_cvt_f32_ubyte1_e32 v159, v151
	v_cvt_f32_ubyte0_e32 v158, v151
	v_pk_mul_f32 v[108:109], v[108:109], v[156:157]
	v_rcp_iflag_f32_e32 v153, v2
	v_cvt_f32_ubyte3_e32 v157, v151
	v_cvt_f32_ubyte2_e32 v156, v151
	v_pk_mul_f32 v[150:151], v[154:155], v[158:159]
	s_waitcnt vmcnt(12)
;     static __device__ __forceinline__ float ub(unsigned w, int k) { return (float)((w >> (8 * k)) & 255u); }
;     __device__ __forceinline__ void mid(f32x4 (&acc)[2][2][4][2], const Unit& u, int t, int wr, int wc, int fr, int fq) const {
;     ...
;         for (int ai = 0; ai < 2; ++ai) { u32x2 ga[4][2], gb[4][2];
; #pragma unroll
;             for (int m = 0; m < 4; ++m)
; #pragma unroll
;                 for (int bj = 0; bj < 2; ++bj) { const unsigned char* p = gp + (size_t)(ai * HALF + m * 16) * ldg + bj * HALF; ga[m][bj] = *(const u32x2*)p; gb[m][bj] = *(const u32x2*)(p + 2048); }
; #pragma unroll
;             for (int m = 0; m < 4; ++m)
; #pragma unroll
;                 for (int bj = 0; bj < 2; ++bj)
; #pragma unroll
;                     for (int h = 0; h < 2; ++h)
; #pragma unroll
;                         for (int k = 0; k < 4; ++k) acc[ai][bj][m][h][k] *= ub(ga[m][bj][h], k) * __builtin_amdgcn_rcpf(ub(gb[m][bj][h], k));
	v_cvt_f32_ubyte0_e32 v2, v148
	v_pk_mul_f32 v[102:103], v[102:103], v[150:151]
	v_rcp_iflag_f32_e32 v150, v2
	v_cvt_f32_ubyte1_e32 v2, v148
	v_rcp_iflag_f32_e32 v151, v2
	v_pk_mul_f32 v[152:153], v[152:153], v[156:157]
	v_cvt_f32_ubyte2_e32 v2, v148
	v_pk_mul_f32 v[104:105], v[104:105], v[152:153]
	v_rcp_iflag_f32_e32 v152, v2
	v_cvt_f32_ubyte3_e32 v2, v148
	v_cvt_f32_ubyte1_e32 v157, v146
	v_cvt_f32_ubyte0_e32 v156, v146
	v_rcp_iflag_f32_e32 v153, v2
	v_pk_mul_f32 v[150:151], v[150:151], v[156:157]
	v_cvt_f32_ubyte0_e32 v2, v149
	v_pk_mul_f32 v[98:99], v[98:99], v[150:151]
	v_rcp_iflag_f32_e32 v150, v2
	v_cvt_f32_ubyte1_e32 v2, v149
	v_rcp_iflag_f32_e32 v151, v2
	v_cvt_f32_ubyte3_e32 v155, v146
	v_cvt_f32_ubyte2_e32 v154, v146
	v_cvt_f32_ubyte2_e32 v2, v149
	v_pk_mul_f32 v[152:153], v[152:153], v[154:155]
	v_rcp_iflag_f32_e32 v148, v2
	v_cvt_f32_ubyte3_e32 v2, v149
	v_cvt_f32_ubyte1_e32 v155, v147
	v_cvt_f32_ubyte0_e32 v154, v147
	v_pk_mul_f32 v[100:101], v[100:101], v[152:153]
	v_rcp_iflag_f32_e32 v149, v2
	v_cvt_f32_ubyte3_e32 v153, v147
	v_cvt_f32_ubyte2_e32 v152, v147
	v_pk_mul_f32 v[146:147], v[150:151], v[154:155]
	v_cvt_f32_ubyte0_e32 v2, v142
	v_pk_mul_f32 v[94:95], v[94:95], v[146:147]
	v_rcp_iflag_f32_e32 v146, v2
	v_cvt_f32_ubyte1_e32 v2, v142
	v_rcp_iflag_f32_e32 v147, v2
	v_pk_mul_f32 v[148:149], v[148:149], v[152:153]
	v_cvt_f32_ubyte2_e32 v2, v142
	v_pk_mul_f32 v[96:97], v[96:97], v[148:149]
	v_rcp_iflag_f32_e32 v148, v2
	v_cvt_f32_ubyte3_e32 v2, v142
	v_cvt_f32_ubyte1_e32 v153, v138
	v_cvt_f32_ubyte0_e32 v152, v138
	v_rcp_iflag_f32_e32 v149, v2
	v_pk_mul_f32 v[146:147], v[146:147], v[152:153]
	v_cvt_f32_ubyte0_e32 v2, v143
	v_pk_mul_f32 v[90:91], v[90:91], v[146:147]
	v_rcp_iflag_f32_e32 v146, v2
	v_cvt_f32_ubyte1_e32 v2, v143
	v_rcp_iflag_f32_e32 v147, v2
	v_cvt_f32_ubyte3_e32 v151, v138
	v_cvt_f32_ubyte2_e32 v150, v138
	v_cvt_f32_ubyte2_e32 v2, v143
	v_pk_mul_f32 v[148:149], v[148:149], v[150:151]
	v_rcp_iflag_f32_e32 v142, v2
	v_cvt_f32_ubyte3_e32 v2, v143
	v_cvt_f32_ubyte1_e32 v151, v139
	v_cvt_f32_ubyte0_e32 v150, v139
	v_pk_mul_f32 v[92:93], v[92:93], v[148:149]
	v_rcp_iflag_f32_e32 v143, v2
	v_cvt_f32_ubyte3_e32 v149, v139
	v_cvt_f32_ubyte2_e32 v148, v139
	v_pk_mul_f32 v[138:139], v[146:147], v[150:151]
	v_cvt_f32_ubyte0_e32 v2, v144
	v_pk_mul_f32 v[86:87], v[86:87], v[138:139]
	v_rcp_iflag_f32_e32 v138, v2
	v_cvt_f32_ubyte1_e32 v2, v144
	v_rcp_iflag_f32_e32 v139, v2
	v_pk_mul_f32 v[142:143], v[142:143], v[148:149]
	v_cvt_f32_ubyte2_e32 v2, v144
	v_pk_mul_f32 v[88:89], v[88:89], v[142:143]
	v_rcp_iflag_f32_e32 v142, v2
	v_cvt_f32_ubyte3_e32 v2, v144
	v_cvt_f32_ubyte1_e32 v149, v140
	v_cvt_f32_ubyte0_e32 v148, v140
	v_rcp_iflag_f32_e32 v143, v2
	v_pk_mul_f32 v[138:139], v[138:139], v[148:149]
	v_cvt_f32_ubyte0_e32 v2, v145
	v_pk_mul_f32 v[82:83], v[82:83], v[138:139]
	v_rcp_iflag_f32_e32 v138, v2
	v_cvt_f32_ubyte1_e32 v2, v145
	v_rcp_iflag_f32_e32 v139, v2
	v_cvt_f32_ubyte3_e32 v147, v140
	v_cvt_f32_ubyte2_e32 v146, v140
	v_pk_mul_f32 v[142:143], v[142:143], v[146:147]
	v_cvt_f32_ubyte2_e32 v2, v145
	v_pk_mul_f32 v[84:85], v[84:85], v[142:143]
	v_rcp_iflag_f32_e32 v142, v2
	v_cvt_f32_ubyte3_e32 v2, v145
	v_cvt_f32_ubyte1_e32 v147, v141
	v_cvt_f32_ubyte0_e32 v146, v141
	v_rcp_iflag_f32_e32 v143, v2
	v_pk_mul_f32 v[138:139], v[138:139], v[146:147]
	v_cvt_f32_ubyte0_e32 v2, v136
	v_pk_mul_f32 v[78:79], v[78:79], v[138:139]
	v_rcp_iflag_f32_e32 v138, v2
	v_cvt_f32_ubyte1_e32 v2, v136
	v_rcp_iflag_f32_e32 v139, v2
	v_cvt_f32_ubyte3_e32 v145, v141
	v_cvt_f32_ubyte2_e32 v144, v141
	v_pk_mul_f32 v[140:141], v[142:143], v[144:145]
	v_cvt_f32_ubyte2_e32 v2, v136
	v_pk_mul_f32 v[80:81], v[80:81], v[140:141]
	v_rcp_iflag_f32_e32 v140, v2
	v_cvt_f32_ubyte3_e32 v2, v136
	v_cvt_f32_ubyte1_e32 v145, v134
	v_cvt_f32_ubyte0_e32 v144, v134
	v_rcp_iflag_f32_e32 v141, v2
	v_pk_mul_f32 v[138:139], v[138:139], v[144:145]
	v_cvt_f32_ubyte0_e32 v2, v137
	v_pk_mul_f32 v[74:75], v[74:75], v[138:139]
	v_rcp_iflag_f32_e32 v138, v2
	v_cvt_f32_ubyte1_e32 v2, v137
	v_rcp_iflag_f32_e32 v139, v2
	v_cvt_f32_ubyte2_e32 v2, v137
	v_rcp_iflag_f32_e32 v136, v2
	v_cvt_f32_ubyte3_e32 v2, v137
	v_rcp_iflag_f32_e32 v137, v2
	v_cvt_f32_ubyte3_e32 v143, v134
	v_cvt_f32_ubyte2_e32 v142, v134
	v_pk_mul_f32 v[140:141], v[140:141], v[142:143]
	v_cvt_f32_ubyte1_e32 v143, v135
	v_pk_mul_f32 v[76:77], v[76:77], v[140:141]
	v_cvt_f32_ubyte3_e32 v141, v135
	v_cvt_f32_ubyte2_e32 v140, v135
	v_cvt_f32_ubyte0_e32 v142, v135
	v_pk_mul_f32 v[134:135], v[138:139], v[142:143]
	v_pk_mul_f32 v[136:137], v[136:137], v[140:141]
	v_pk_mul_f32 v[70:71], v[70:71], v[134:135]
	v_pk_mul_f32 v[72:73], v[72:73], v[136:137]
	v_add_co_u32_e32 v134, vcc, s0, v4
	s_mov_b32 s0, 0x3f0000
	s_nop 0
	v_addc_co_u32_e32 v135, vcc, 0, v5, vcc
	v_add_co_u32_e32 v134, vcc, s0, v4
	s_mov_b32 s0, 0x460000
	s_nop 0
	v_addc_co_u32_e32 v135, vcc, 0, v5, vcc
	v_add_co_u32_e32 v134, vcc, s0, v4
	s_mov_b32 s0, 0x4d0000
	s_nop 0
	v_addc_co_u32_e32 v135, vcc, 0, v5, vcc
	v_add_co_u32_e32 v134, vcc, s0, v4
	s_waitcnt vmcnt(0)
;     static __device__ __forceinline__ float ub(unsigned w, int k) { return (float)((w >> (8 * k)) & 255u); }
;     __device__ __forceinline__ void mid(f32x4 (&acc)[2][2][4][2], const Unit& u, int t, int wr, int wc, int fr, int fq) const {
;     ...
;         for (int ai = 0; ai < 2; ++ai) { u32x2 ga[4][2], gb[4][2];
; #pragma unroll
;             for (int m = 0; m < 4; ++m)
; #pragma unroll
;                 for (int bj = 0; bj < 2; ++bj) { const unsigned char* p = gp + (size_t)(ai * HALF + m * 16) * ldg + bj * HALF; ga[m][bj] = *(const u32x2*)p; gb[m][bj] = *(const u32x2*)(p + 2048); }
; #pragma unroll
;             for (int m = 0; m < 4; ++m)
; #pragma unroll
;                 for (int bj = 0; bj < 2; ++bj)
; #pragma unroll
;                     for (int h = 0; h < 2; ++h)
; #pragma unroll
;                         for (int k = 0; k < 4; ++k) acc[ai][bj][m][h][k] *= ub(ga[m][bj][h], k) * __builtin_amdgcn_rcpf(ub(gb[m][bj][h], k));
	v_cvt_f32_ubyte1_e32 v171, v174
	v_addc_co_u32_e32 v135, vcc, 0, v5, vcc
	global_load_dwordx2 v[136:137], v[134:135], off
	global_load_dwordx2 v[138:139], v[134:135], off offset:2048
	global_load_dwordx2 v[4:5], v[134:135], off offset:128
	s_nop 0
	global_load_dwordx2 v[134:135], v[134:135], off offset:2176
	v_cvt_f32_ubyte0_e32 v2, v176
	v_rcp_iflag_f32_e32 v164, v2
	v_cvt_f32_ubyte1_e32 v2, v176
	v_rcp_iflag_f32_e32 v165, v2
	v_cvt_f32_ubyte2_e32 v2, v176
	v_rcp_iflag_f32_e32 v166, v2
	v_cvt_f32_ubyte3_e32 v2, v176
	v_cvt_f32_ubyte0_e32 v170, v174
	v_rcp_iflag_f32_e32 v167, v2
	v_pk_mul_f32 v[164:165], v[164:165], v[170:171]
	v_cvt_f32_ubyte0_e32 v2, v177
	v_pk_mul_f32 v[66:67], v[66:67], v[164:165]
	v_rcp_iflag_f32_e32 v164, v2
	v_cvt_f32_ubyte1_e32 v2, v177
	v_rcp_iflag_f32_e32 v165, v2
	v_cvt_f32_ubyte3_e32 v169, v174
	v_cvt_f32_ubyte2_e32 v168, v174
	v_cvt_f32_ubyte2_e32 v2, v177
	v_pk_mul_f32 v[166:167], v[166:167], v[168:169]
	v_rcp_iflag_f32_e32 v150, v2
	v_cvt_f32_ubyte3_e32 v2, v177
	v_cvt_f32_ubyte1_e32 v169, v175
	v_cvt_f32_ubyte0_e32 v168, v175
	v_pk_mul_f32 v[68:69], v[68:69], v[166:167]
	v_rcp_iflag_f32_e32 v151, v2
	v_cvt_f32_ubyte3_e32 v167, v175
	v_cvt_f32_ubyte2_e32 v166, v175
	v_pk_mul_f32 v[148:149], v[164:165], v[168:169]
	v_cvt_f32_ubyte0_e32 v2, v180
	v_pk_mul_f32 v[62:63], v[62:63], v[148:149]
	v_rcp_iflag_f32_e32 v148, v2
	v_cvt_f32_ubyte1_e32 v2, v180
	v_rcp_iflag_f32_e32 v149, v2
	v_pk_mul_f32 v[150:151], v[150:151], v[166:167]
	v_cvt_f32_ubyte2_e32 v2, v180
	v_pk_mul_f32 v[64:65], v[64:65], v[150:151]
	v_rcp_iflag_f32_e32 v150, v2
	v_cvt_f32_ubyte3_e32 v2, v180
	v_cvt_f32_ubyte1_e32 v167, v178
	v_cvt_f32_ubyte0_e32 v166, v178
	v_rcp_iflag_f32_e32 v151, v2
	v_pk_mul_f32 v[148:149], v[148:149], v[166:167]
	v_cvt_f32_ubyte0_e32 v2, v181
	v_pk_mul_f32 v[58:59], v[58:59], v[148:149]
	v_rcp_iflag_f32_e32 v148, v2
	v_cvt_f32_ubyte1_e32 v2, v181
	v_rcp_iflag_f32_e32 v149, v2
	v_cvt_f32_ubyte3_e32 v165, v178
	v_cvt_f32_ubyte2_e32 v164, v178
	v_pk_mul_f32 v[150:151], v[150:151], v[164:165]
	v_cvt_f32_ubyte2_e32 v2, v181
	v_pk_mul_f32 v[60:61], v[60:61], v[150:151]
	v_rcp_iflag_f32_e32 v150, v2
	v_cvt_f32_ubyte3_e32 v2, v181
	v_cvt_f32_ubyte1_e32 v165, v179
	v_cvt_f32_ubyte0_e32 v164, v179
	v_rcp_iflag_f32_e32 v151, v2
	v_pk_mul_f32 v[148:149], v[148:149], v[164:165]
	v_cvt_f32_ubyte0_e32 v2, v184
	v_pk_mul_f32 v[54:55], v[54:55], v[148:149]
	v_rcp_iflag_f32_e32 v148, v2
	v_cvt_f32_ubyte1_e32 v2, v184
	v_rcp_iflag_f32_e32 v149, v2
	v_cvt_f32_ubyte3_e32 v155, v179
	v_cvt_f32_ubyte2_e32 v154, v179
	v_pk_mul_f32 v[150:151], v[150:151], v[154:155]
	v_cvt_f32_ubyte2_e32 v2, v184
	v_pk_mul_f32 v[56:57], v[56:57], v[150:151]
	v_rcp_iflag_f32_e32 v150, v2
	v_cvt_f32_ubyte3_e32 v2, v184
	v_cvt_f32_ubyte1_e32 v155, v182
	v_cvt_f32_ubyte0_e32 v154, v182
	v_rcp_iflag_f32_e32 v151, v2
	v_pk_mul_f32 v[148:149], v[148:149], v[154:155]
	v_cvt_f32_ubyte0_e32 v2, v185
	v_pk_mul_f32 v[50:51], v[50:51], v[148:149]
	v_rcp_iflag_f32_e32 v148, v2
	v_cvt_f32_ubyte1_e32 v2, v185
	v_rcp_iflag_f32_e32 v149, v2
	v_cvt_f32_ubyte3_e32 v153, v182
	v_cvt_f32_ubyte2_e32 v152, v182
	v_pk_mul_f32 v[150:151], v[150:151], v[152:153]
	v_cvt_f32_ubyte2_e32 v2, v185
	v_pk_mul_f32 v[52:53], v[52:53], v[150:151]
	v_rcp_iflag_f32_e32 v150, v2
	v_cvt_f32_ubyte3_e32 v2, v185
	v_cvt_f32_ubyte1_e32 v155, v183
	v_cvt_f32_ubyte0_e32 v154, v183
	v_rcp_iflag_f32_e32 v151, v2
	v_pk_mul_f32 v[148:149], v[148:149], v[154:155]
	v_cvt_f32_ubyte0_e32 v2, v188
	v_pk_mul_f32 v[46:47], v[46:47], v[148:149]
	v_rcp_iflag_f32_e32 v148, v2
	v_cvt_f32_ubyte1_e32 v2, v188
	v_rcp_iflag_f32_e32 v149, v2
	v_cvt_f32_ubyte3_e32 v153, v183
	v_cvt_f32_ubyte2_e32 v152, v183
	v_pk_mul_f32 v[150:151], v[150:151], v[152:153]
	v_cvt_f32_ubyte2_e32 v2, v188
	v_pk_mul_f32 v[48:49], v[48:49], v[150:151]
	v_rcp_iflag_f32_e32 v150, v2
	v_cvt_f32_ubyte3_e32 v2, v188
	v_cvt_f32_ubyte1_e32 v155, v186
	v_cvt_f32_ubyte0_e32 v154, v186
	v_rcp_iflag_f32_e32 v151, v2
	v_pk_mul_f32 v[148:149], v[148:149], v[154:155]
	v_cvt_f32_ubyte0_e32 v2, v189
	v_pk_mul_f32 v[42:43], v[42:43], v[148:149]
	v_rcp_iflag_f32_e32 v148, v2
	v_cvt_f32_ubyte1_e32 v2, v189
	v_rcp_iflag_f32_e32 v149, v2
	v_cvt_f32_ubyte3_e32 v153, v186
	v_cvt_f32_ubyte2_e32 v152, v186
	v_pk_mul_f32 v[150:151], v[150:151], v[152:153]
	v_cvt_f32_ubyte2_e32 v2, v189
	v_pk_mul_f32 v[44:45], v[44:45], v[150:151]
	v_rcp_iflag_f32_e32 v150, v2
	v_cvt_f32_ubyte3_e32 v2, v189
	v_cvt_f32_ubyte1_e32 v155, v187
	v_cvt_f32_ubyte0_e32 v154, v187
	v_rcp_iflag_f32_e32 v151, v2
	v_pk_mul_f32 v[148:149], v[148:149], v[154:155]
	v_cvt_f32_ubyte0_e32 v2, v192
	v_pk_mul_f32 v[38:39], v[38:39], v[148:149]
	v_rcp_iflag_f32_e32 v148, v2
	v_cvt_f32_ubyte1_e32 v2, v192
	v_rcp_iflag_f32_e32 v149, v2
	v_cvt_f32_ubyte3_e32 v153, v187
	v_cvt_f32_ubyte2_e32 v152, v187
	v_pk_mul_f32 v[150:151], v[150:151], v[152:153]
	v_cvt_f32_ubyte2_e32 v2, v192
	v_pk_mul_f32 v[40:41], v[40:41], v[150:151]
	v_rcp_iflag_f32_e32 v150, v2
	v_cvt_f32_ubyte3_e32 v2, v192
	v_cvt_f32_ubyte1_e32 v155, v190
	v_cvt_f32_ubyte0_e32 v154, v190
	v_rcp_iflag_f32_e32 v151, v2
	v_pk_mul_f32 v[148:149], v[148:149], v[154:155]
	v_cvt_f32_ubyte0_e32 v2, v193
	v_pk_mul_f32 v[34:35], v[34:35], v[148:149]
	v_rcp_iflag_f32_e32 v148, v2
	v_cvt_f32_ubyte1_e32 v2, v193
	v_rcp_iflag_f32_e32 v149, v2
	v_cvt_f32_ubyte3_e32 v153, v190
	v_cvt_f32_ubyte2_e32 v152, v190
	v_cvt_f32_ubyte2_e32 v2, v193
	v_pk_mul_f32 v[150:151], v[150:151], v[152:153]
	v_rcp_iflag_f32_e32 v146, v2
	v_cvt_f32_ubyte3_e32 v2, v193
	v_cvt_f32_ubyte1_e32 v153, v191
	v_cvt_f32_ubyte0_e32 v152, v191
	v_pk_mul_f32 v[36:37], v[36:37], v[150:151]
	v_rcp_iflag_f32_e32 v147, v2
	v_cvt_f32_ubyte3_e32 v151, v191
	v_cvt_f32_ubyte2_e32 v150, v191
	v_pk_mul_f32 v[144:145], v[148:149], v[152:153]
	v_cvt_f32_ubyte0_e32 v2, v196
	v_pk_mul_f32 v[30:31], v[30:31], v[144:145]
	v_rcp_iflag_f32_e32 v144, v2
	v_cvt_f32_ubyte1_e32 v2, v196
	v_rcp_iflag_f32_e32 v145, v2
	v_pk_mul_f32 v[146:147], v[146:147], v[150:151]
	v_cvt_f32_ubyte2_e32 v2, v196
	v_pk_mul_f32 v[32:33], v[32:33], v[146:147]
	v_rcp_iflag_f32_e32 v146, v2
	v_cvt_f32_ubyte3_e32 v2, v196
	v_cvt_f32_ubyte1_e32 v151, v194
	v_cvt_f32_ubyte0_e32 v150, v194
	v_rcp_iflag_f32_e32 v147, v2
	v_pk_mul_f32 v[144:145], v[144:145], v[150:151]
	v_cvt_f32_ubyte0_e32 v2, v197
	v_pk_mul_f32 v[26:27], v[26:27], v[144:145]
	v_rcp_iflag_f32_e32 v144, v2
	v_cvt_f32_ubyte1_e32 v2, v197
	v_rcp_iflag_f32_e32 v145, v2
	v_cvt_f32_ubyte3_e32 v149, v194
	v_cvt_f32_ubyte2_e32 v148, v194
	v_cvt_f32_ubyte2_e32 v2, v197
	v_pk_mul_f32 v[146:147], v[146:147], v[148:149]
	v_rcp_iflag_f32_e32 v142, v2
	v_cvt_f32_ubyte3_e32 v2, v197
	v_cvt_f32_ubyte1_e32 v149, v195
	v_cvt_f32_ubyte0_e32 v148, v195
	v_pk_mul_f32 v[28:29], v[28:29], v[146:147]
	v_rcp_iflag_f32_e32 v143, v2
	v_cvt_f32_ubyte3_e32 v147, v195
	v_cvt_f32_ubyte2_e32 v146, v195
	v_pk_mul_f32 v[140:141], v[144:145], v[148:149]
	s_waitcnt vmcnt(0)
;     static __device__ __forceinline__ float ub(unsigned w, int k) { return (float)((w >> (8 * k)) & 255u); }
;     __device__ __forceinline__ void mid(f32x4 (&acc)[2][2][4][2], const Unit& u, int t, int wr, int wc, int fr, int fq) const {
;     ...
;         for (int ai = 0; ai < 2; ++ai) { u32x2 ga[4][2], gb[4][2];
; #pragma unroll
;             for (int m = 0; m < 4; ++m)
; #pragma unroll
;                 for (int bj = 0; bj < 2; ++bj) { const unsigned char* p = gp + (size_t)(ai * HALF + m * 16) * ldg + bj * HALF; ga[m][bj] = *(const u32x2*)p; gb[m][bj] = *(const u32x2*)(p + 2048); }
; #pragma unroll
;             for (int m = 0; m < 4; ++m)
; #pragma unroll
;                 for (int bj = 0; bj < 2; ++bj)
; #pragma unroll
;                     for (int h = 0; h < 2; ++h)
; #pragma unroll
;                         for (int k = 0; k < 4; ++k) acc[ai][bj][m][h][k] *= ub(ga[m][bj][h], k) * __builtin_amdgcn_rcpf(ub(gb[m][bj][h], k));
	v_cvt_f32_ubyte0_e32 v2, v138
	v_pk_mul_f32 v[22:23], v[22:23], v[140:141]
	v_rcp_iflag_f32_e32 v140, v2
	v_cvt_f32_ubyte1_e32 v2, v138
	v_rcp_iflag_f32_e32 v141, v2
	v_pk_mul_f32 v[142:143], v[142:143], v[146:147]
	v_cvt_f32_ubyte2_e32 v2, v138
	v_pk_mul_f32 v[24:25], v[24:25], v[142:143]
	v_rcp_iflag_f32_e32 v142, v2
	v_cvt_f32_ubyte3_e32 v2, v138
	v_cvt_f32_ubyte1_e32 v147, v136
	v_cvt_f32_ubyte0_e32 v146, v136
	v_rcp_iflag_f32_e32 v143, v2
	v_pk_mul_f32 v[140:141], v[140:141], v[146:147]
	v_cvt_f32_ubyte0_e32 v2, v139
	v_pk_mul_f32 v[18:19], v[18:19], v[140:141]
	v_rcp_iflag_f32_e32 v140, v2
	v_cvt_f32_ubyte1_e32 v2, v139
	v_rcp_iflag_f32_e32 v141, v2
	v_cvt_f32_ubyte3_e32 v145, v136
	v_cvt_f32_ubyte2_e32 v144, v136
	v_cvt_f32_ubyte2_e32 v2, v139
	v_pk_mul_f32 v[142:143], v[142:143], v[144:145]
	v_rcp_iflag_f32_e32 v138, v2
	v_cvt_f32_ubyte3_e32 v2, v139
	v_cvt_f32_ubyte1_e32 v145, v137
	v_cvt_f32_ubyte0_e32 v144, v137
	v_pk_mul_f32 v[20:21], v[20:21], v[142:143]
	v_rcp_iflag_f32_e32 v139, v2
	v_cvt_f32_ubyte3_e32 v143, v137
	v_cvt_f32_ubyte2_e32 v142, v137
	v_pk_mul_f32 v[136:137], v[140:141], v[144:145]
	v_cvt_f32_ubyte0_e32 v2, v134
	v_pk_mul_f32 v[14:15], v[14:15], v[136:137]
	v_rcp_iflag_f32_e32 v136, v2
	v_cvt_f32_ubyte1_e32 v2, v134
	v_rcp_iflag_f32_e32 v137, v2
	v_pk_mul_f32 v[138:139], v[138:139], v[142:143]
	v_cvt_f32_ubyte2_e32 v2, v134
	v_pk_mul_f32 v[16:17], v[16:17], v[138:139]
	v_rcp_iflag_f32_e32 v138, v2
	v_cvt_f32_ubyte3_e32 v2, v134
	v_cvt_f32_ubyte1_e32 v143, v4
	v_cvt_f32_ubyte0_e32 v142, v4
	v_rcp_iflag_f32_e32 v139, v2
	v_pk_mul_f32 v[136:137], v[136:137], v[142:143]
	v_cvt_f32_ubyte0_e32 v2, v135
	v_pk_mul_f32 v[10:11], v[10:11], v[136:137]
	v_rcp_iflag_f32_e32 v136, v2
	v_cvt_f32_ubyte1_e32 v2, v135
	v_rcp_iflag_f32_e32 v137, v2
	v_cvt_f32_ubyte2_e32 v2, v135
	v_rcp_iflag_f32_e32 v134, v2
	v_cvt_f32_ubyte3_e32 v2, v135
	v_rcp_iflag_f32_e32 v135, v2
	v_cvt_f32_ubyte3_e32 v141, v4
	v_cvt_f32_ubyte2_e32 v140, v4
	v_pk_mul_f32 v[138:139], v[138:139], v[140:141]
	v_cvt_f32_ubyte1_e32 v141, v5
	v_pk_mul_f32 v[12:13], v[12:13], v[138:139]
	v_cvt_f32_ubyte3_e32 v139, v5
	v_cvt_f32_ubyte2_e32 v138, v5
	v_cvt_f32_ubyte0_e32 v140, v5
	v_pk_mul_f32 v[4:5], v[136:137], v[140:141]
	v_pk_mul_f32 v[134:135], v[134:135], v[138:139]
	v_pk_mul_f32 v[6:7], v[6:7], v[4:5]
	v_pk_mul_f32 v[8:9], v[8:9], v[134:135]
	s_nop 0

; #define GAS __attribute__((address_space(1)))
; __device__ __forceinline__ void resid_rows(bf16* X, const bf16* Y, const float* PART, const float* gpost, float* RSv, float* RQv, float* fout, unsigned char* XQv, int m0, int mstep, int lane, int M_end = M) {
;     ...
;     f32x4 g[8];
;     { const GAS f32x4* gp = (const GAS f32x4*)gpost + lane;
; #pragma unroll
;       for (int j = 0; j < 8; ++j) g[j] = gp[64 * j]; }
;     v2u cx[8], cy[8], nx[8], ny[8]; float cp = 0.f, np = 0.f;
;     int m = m0;
;     if (m < M) { const GAS v2u* xr = (const GAS v2u*)(X + (size_t)m * DM) + lane; const GAS v2u* yr = (const GAS v2u*)(Y + (size_t)m * DM) + lane; cp = (lane < 32) ? PART[(size_t)m * 32 + lane] : 0.f;
; #pragma unroll
;         for (int j = 0; j < 8; ++j) { cx[j] = xr[64 * j]; cy[j] = yr[64 * j]; } }
.LBB0_1003:
	s_andn2_b64 vcc, exec, s[38:39]
	s_cbranch_vccnz .LBB0_1103
	v_readlane_b32 s0, v255, 26
	v_mov_b32_e32 v1, v234
	s_lshl_b32 s34, s0, 11
	v_readlane_b32 s36, v250, 2
	s_lshl_b64 s[4:5], s[34:35], 2
	v_readlane_b32 s42, v250, 8
	v_and_b32_e32 v1, 63, v1
	v_readlane_b32 s43, v250, 9
	s_add_u32 s4, s42, s4
	s_addc_u32 s5, s43, s5
	v_lshlrev_b32_e32 v2, 4, v1
	s_waitcnt vmcnt(0)
	v_lshl_add_u64 v[20:21], s[4:5], 0, v[2:3]
	v_add_co_u32_e32 v32, vcc, 0x1000, v20
	s_waitcnt lgkmcnt(0)
	global_load_dwordx4 v[4:7], v2, s[4:5]
	global_load_dwordx4 v[8:11], v2, s[4:5] offset:1024
	global_load_dwordx4 v[12:15], v2, s[4:5] offset:2048
	global_load_dwordx4 v[16:19], v2, s[4:5] offset:3072
	v_addc_co_u32_e32 v33, vcc, 0, v21, vcc
	global_load_dwordx4 v[20:23], v[32:33], off
	global_load_dwordx4 v[24:27], v[32:33], off offset:1024
	global_load_dwordx4 v[28:31], v[32:33], off offset:2048
	s_nop 0
	global_load_dwordx4 v[32:35], v[32:33], off offset:3072
	v_readlane_b32 s4, v250, 50
	v_readlane_b32 s38, v250, 4
	v_readlane_b32 s39, v250, 5
	v_readlane_b32 s5, v250, 51
	s_mov_b64 s[38:39], -1
	s_and_b64 vcc, exec, s[4:5]
	v_readlane_b32 s37, v250, 3
	v_readlane_b32 s40, v250, 6
	v_readlane_b32 s41, v250, 7
	v_readlane_b32 s44, v250, 10
	v_readlane_b32 s45, v250, 11
	v_readlane_b32 s46, v250, 12
	v_readlane_b32 s47, v250, 13
	v_readlane_b32 s48, v250, 14
	v_readlane_b32 s49, v250, 15
	v_readlane_b32 s50, v250, 16
	v_readlane_b32 s51, v250, 17
	s_cbranch_vccz .LBB0_1017
	v_readlane_b32 s4, v253, 23
	v_readlane_b32 s5, v253, 24
	v_readlane_b32 s24, v254, 37
	v_readlane_b32 s36, v254, 39
	s_andn2_b64 vcc, exec, s[4:5]
	v_readlane_b32 s25, v254, 38
	v_readlane_b32 s37, v254, 40
	s_cbranch_vccnz .LBB0_1016
	v_cmp_gt_u32_e64 s[38:39], 32, v1
	v_mov_b32_e32 v110, 0
	v_mov_b32_e32 v108, 0
	s_and_saveexec_b64 s[40:41], s[38:39]
	s_cbranch_execz .LBB0_1008
	v_readlane_b32 s4, v253, 33
	v_lshlrev_b32_e32 v2, 2, v1
	v_readlane_b32 s5, v253, 34
	s_nop 4
	global_load_dword v108, v2, s[4:5]

; #define GAS __attribute__((address_space(1)))
; __device__ __forceinline__ void resid_rows(bf16* X, const bf16* Y, const float* PART, const float* gpost, float* RSv, float* RQv, float* fout, unsigned char* XQv, int m0, int mstep, int lane, int M_end = M) {
;     ...
;     f32x4 g[8];
;     { const GAS f32x4* gp = (const GAS f32x4*)gpost + lane;
; #pragma unroll
;       for (int j = 0; j < 8; ++j) g[j] = gp[64 * j]; }
;     v2u cx[8], cy[8], nx[8], ny[8]; float cp = 0.f, np = 0.f;
;     int m = m0;
;     if (m < M) { const GAS v2u* xr = (const GAS v2u*)(X + (size_t)m * DM) + lane; const GAS v2u* yr = (const GAS v2u*)(Y + (size_t)m * DM) + lane; cp = (lane < 32) ? PART[(size_t)m * 32 + lane] : 0.f;
; #pragma unroll
;         for (int j = 0; j < 8; ++j) { cx[j] = xr[64 * j]; cy[j] = yr[64 * j]; } }
.LBB0_1017:
	v_readlane_b32 s50, v255, 22
	s_andn2_b64 vcc, exec, s[38:39]
	v_readlane_b32 s51, v255, 23
	s_cbranch_vccnz .LBB0_1029
	v_readlane_b32 s4, v253, 36
	v_readlane_b32 s5, v253, 37
	s_andn2_b64 vcc, exec, s[4:5]
	s_cbranch_vccnz .LBB0_1029
	v_cmp_gt_u32_e64 s[38:39], 32, v1
	v_mov_b32_e32 v110, 0
	v_lshlrev_b32_e32 v40, 2, v1
	v_mov_b32_e32 v108, 0
	s_and_saveexec_b64 s[40:41], s[38:39]
	s_cbranch_execz .LBB0_1021
	v_readlane_b32 s4, v253, 44
	v_readlane_b32 s5, v253, 45
	s_nop 4
	global_load_dword v108, v40, s[4:5]
